# MoE gate/up GEMM unit head: the drain wait in front of the four gather-offset loads dropped (they overlap with the store drain; one wait behind them)
# baseline (speedup 1.0000x reference)
; #define PROB_WS() unsigned char* w_ = ws; asm volatile("" : "+s"(w_))
;     __device__ __forceinline__ void a_offs(const Unit& u, unsigned (&off)[2][2], const int (&sR)[2], const int (&sC)[2]) const { const int e = u.e, lt = u.lt; const int cnt = mt.p[32 + e];
;         PROB_WS(); const int* rowtok = (const int*)(w_ + WS_ROWTOK);
; #pragma unroll
;         for (int h = 0; h < 2; ++h)
; #pragma unroll
;             for (int i2 = 0; i2 < 2; ++i2) { const int idx = lt * 256 + h * 128 + sR[i2]; const int tok = idx < cnt ? (rowtok[(size_t)e * MT + idx] >> 1) : 0; off[h][i2] = (unsigned)(tok * 512 + sC[i2]) * 2u; } }
.LBB0_1596:
	s_and_b64 vcc, exec, s[38:39]
	v_mov_b32_e32 v190, v168
	v_mov_b32_e32 v189, v170
	v_mov_b32_e32 v191, v172
	v_mov_b32_e32 v192, v174
	s_cbranch_vccnz .LBB0_1606
	s_lshl_b32 s3, s42, 2
	s_add_i32 s3, s3, 0
	s_add_i32 s3, s3, 0x22900
	v_mov_b32_e32 v4, s3
	ds_read_b32 v8, v4
	s_ashr_i32 s43, s42, 31
	s_mov_b64 s[26:27], s[4:5]
	s_lshl_b64 s[34:35], s[42:43], 16
	s_add_u32 s3, s26, s34
	v_lshlrev_b32_e32 v11, 8, v188
	s_addc_u32 s13, s27, s35
	s_add_u32 s50, s3, 0x5f4000
	v_add_u32_e32 v4, v11, v1
	s_addc_u32 s51, s13, 0
	s_waitcnt lgkmcnt(0)
	v_cmp_lt_i32_e32 vcc, v4, v8
	v_mov_b32_e32 v14, 0
	v_mov_b32_e32 v15, 0
	v_mov_b32_e32 v16, 0
	v_mov_b32_e32 v17, 0
	v_ashrrev_i32_e32 v5, 31, v4
	s_and_saveexec_b64 s[52:53], vcc
	s_cbranch_execz .Laoffs_u1
	v_lshl_add_u64 v[18:19], v[4:5], 2, s[50:51]
	flat_load_dword v14, v[18:19]
